# speedup vs baseline: 1.0027x; 1.0027x over previous
_Z11attn_kernelILi0EEvPKDF16_S1_S1_PKfS3_PfPDF16_:
	v_readfirstlane_b32 s3, v0
	s_lshr_b32 s14, s3, 6
	s_lshl_b32 s3, s2, 7
	s_lshr_b32 s12, s2, 4
	s_and_b32 s3, s3, 0x780
	s_lshl_b32 s4, s14, 5
	s_mov_b32 s13, 0
	s_load_dwordx4 s[8:11], s[0:1], 0x0
	s_load_dwordx2 s[18:19], s[0:1], 0x10
	s_add_i32 s3, s4, s3
	s_lshl_b64 s[4:5], s[12:13], 11
	s_add_u32 s16, s4, s3
	s_addc_u32 s17, s5, 0
	s_lshl_b64 s[4:5], s[16:17], 7
	v_and_b32_e32 v164, 31, v0
	s_waitcnt lgkmcnt(0)
	s_add_u32 s4, s8, s4
	v_bfe_u32 v72, v0, 5, 1
	s_addc_u32 s5, s9, s5
	s_lshl_b64 s[22:23], s[12:13], 18
	v_lshlrev_b32_e32 v128, 7, v164
	v_mov_b32_e32 v129, 0
	s_add_u32 s8, s10, s22
	v_lshl_add_u64 v[2:3], s[4:5], 0, v[128:129]
	v_lshlrev_b32_e32 v128, 4, v72
	s_addc_u32 s9, s11, s23
	v_lshl_add_u64 v[10:11], v[2:3], 0, v[128:129]
	v_or_b32_e32 v12, 0x100, v0
	v_lshlrev_b32_e32 v128, 4, v0
	v_lshlrev_b32_e32 v44, 4, v12
	global_load_dwordx4 v[2:5], v128, s[8:9]
	global_load_dwordx4 v[6:9], v44, s[8:9]
	v_lshlrev_b32_e32 v79, 3, v0
	s_movk_i32 s4, 0x48
	v_lshrrev_b32_e32 v73, 3, v0
	v_and_b32_e32 v74, 56, v79
	v_lshrrev_b32_e32 v75, 3, v12
	v_mad_u32_u24 v165, v75, s4, v74
	v_mad_u32_u24 v166, v73, s4, v74
	global_load_dwordx4 v[108:111], v[10:11], off
	global_load_dwordx4 v[104:107], v[10:11], off offset:32
	global_load_dwordx4 v[100:103], v[10:11], off offset:64
	global_load_dwordx4 v[96:99], v[10:11], off offset:96
	v_mov_b32_e32 v86, v44
	s_add_u32 s24, s8, 0x2000
	s_addc_u32 s25, s9, 0
	global_load_dwordx4 v[120:123], v128, s[24:25]
	global_load_dwordx4 v[124:127], v44, s[24:25]
	s_add_u32 s24, s24, 0x2000
	s_addc_u32 s25, s25, 0
	global_load_dwordx4 v[146:149], v128, s[24:25]
	global_load_dwordx4 v[150:153], v44, s[24:25]
	s_add_u32 s24, s24, 0x2000
	s_addc_u32 s25, s25, 0
	global_load_dwordx4 v[154:157], v128, s[24:25]
	global_load_dwordx4 v[158:161], v44, s[24:25]
	s_add_u32 s24, s24, 0x2000
	s_addc_u32 s25, s25, 0
	s_add_u32 s4, s8, 0x2000
	v_lshlrev_b32_e32 v13, 1, v166
	s_addc_u32 s5, s9, 0
	v_lshlrev_b32_e32 v14, 1, v165
	v_lshlrev_b32_e32 v1, 3, v72
	v_mul_u32_u24_e32 v76, 0x48, v164
	v_lshlrev_b32_e32 v80, 3, v12
	v_mov_b32_e32 v45, v129
	s_mov_b32 s15, 1
	v_add_u32_e32 v77, 0x6000, v13
	v_add_u32_e32 v78, 0x6000, v14
	s_waitcnt vmcnt(11)
	ds_write_b128 v13, v[2:5] offset:24576
	s_waitcnt vmcnt(10)
	ds_write_b128 v14, v[6:9] offset:24576
	s_waitcnt lgkmcnt(0)
	s_barrier
	s_load_dwordx4 s[4:7], s[0:1], 0x28
	v_add_lshl_u32 v3, v1, v76, 1
	v_lshl_add_u64 v[68:69], s[8:9], 0, v[44:45]
	v_lshl_add_u64 v[66:67], s[8:9], 0, v[128:129]
	v_add_u32_e32 v167, 0x6000, v3
	v_mov_b32_e32 v87, v3
	v_lshlrev_b32_e32 v88, 1, v166
	v_lshlrev_b32_e32 v89, 1, v165
	s_lshl_b64 s[20:21], s[12:13], 17
	v_mov_b32_e32 v81, 0
	v_mov_b32_e32 v82, 0
	v_mov_b32_e32 v130, 0
	v_mov_b32_e32 v131, 0
	v_mov_b32_e32 v132, 0
	v_mov_b32_e32 v133, 0
	v_mov_b32_e32 v134, 0
	v_mov_b32_e32 v135, 0
	v_mov_b32_e32 v136, 0
	v_mov_b32_e32 v137, 0
	v_mov_b32_e32 v138, 0
	v_mov_b32_e32 v139, 0
	v_mov_b32_e32 v140, 0
	v_mov_b32_e32 v141, 0
	v_mov_b32_e32 v142, 0
	v_mov_b32_e32 v143, 0
	v_mov_b32_e32 v144, 0
	v_mov_b32_e32 v145, 0
	v_mov_b32_e32 v34, 0xff800000
	v_mov_b32_e32 v35, v34
	v_mov_b32_e32 v36, v34
	v_mov_b32_e32 v37, v34
	v_mov_b32_e32 v38, v34
	v_mov_b32_e32 v39, v34
	v_mov_b32_e32 v40, v34
	v_mov_b32_e32 v41, v34
	v_mov_b32_e32 v42, v34
	v_mov_b32_e32 v43, v34
	v_mov_b32_e32 v44, v34
	v_mov_b32_e32 v45, v34
	v_mov_b32_e32 v46, v34
	v_mov_b32_e32 v47, v34
	v_mov_b32_e32 v48, v34
	v_mov_b32_e32 v49, v34
	v_mov_b32_e32 v50, v34
	v_mov_b32_e32 v51, v34
	v_mov_b32_e32 v52, v34
	v_mov_b32_e32 v53, v34
	v_mov_b32_e32 v54, v34
	v_mov_b32_e32 v55, v34
	v_mov_b32_e32 v56, v34
	v_mov_b32_e32 v57, v34
	v_mov_b32_e32 v58, v34
	v_mov_b32_e32 v59, v34
	v_mov_b32_e32 v60, v34
	v_mov_b32_e32 v61, v34
	v_mov_b32_e32 v62, v34
	v_mov_b32_e32 v63, v34
	v_mov_b32_e32 v64, v34
	v_mov_b32_e32 v65, v34
	s_mov_b32 s11, 0xff800000
	s_mov_b32 s15, 0
	s_waitcnt vmcnt(4) lgkmcnt(0)
	ds_write_b128 v77, v[120:123] offset:9216
	ds_write_b128 v78, v[124:127] offset:9216
	s_waitcnt lgkmcnt(0)
	s_barrier
	s_lshl_b32 s30, s2, 20
	s_lshl_b32 s31, s14, 18
	s_add_u32 s30, s30, s31
	s_add_u32 s30, s4, s30
	s_addc_u32 s31, s5, 0
	v_and_b32_e32 v90, 63, v0
	v_lshlrev_b32_e32 v90, 4, v90
	v_mov_b32_e32 v92, 0
	v_mov_b32_e32 v93, 0
	v_mov_b32_e32 v94, 0
	v_mov_b32_e32 v95, 0
	s_waitcnt vmcnt(0)
.Lp1_loop:
	s_waitcnt vmcnt(2)
	ds_write_b128 v88, v[146:149]
	ds_write_b128 v89, v[150:153]
	ds_write_b128 v88, v[154:157] offset:9216
	ds_write_b128 v89, v[158:161] offset:9216
	global_load_dwordx4 v[112:115], v128, s[24:25]
	global_load_dwordx4 v[116:119], v86, s[24:25]
	s_add_u32 s24, s24, 0x2000
	s_addc_u32 s25, s25, 0
	global_load_dwordx4 v[120:123], v128, s[24:25]
	global_load_dwordx4 v[124:127], v86, s[24:25]
	s_add_u32 s24, s24, 0x2000
	s_addc_u32 s25, s25, 0
	global_store_dwordx4 v90, v[92:95], s[30:31]
	s_add_u32 s30, s30, 0x2000
	s_addc_u32 s31, s31, 0
	global_store_dwordx4 v90, v[92:95], s[30:31]
	s_add_u32 s30, s30, 0x2000
	s_addc_u32 s31, s31, 0
	ds_read_b128 v[168:171], v167
	ds_read_b128 v[172:175], v167 offset:4608
	ds_read_b128 v[176:179], v167 offset:32
	ds_read_b128 v[180:183], v167 offset:4640
	ds_read_b128 v[184:187], v167 offset:64
	ds_read_b128 v[188:191], v167 offset:4672
	ds_read_b128 v[192:195], v167 offset:96
	ds_read_b128 v[196:199], v167 offset:4704
	v_mov_b32_e32 v200, 0
	v_mov_b32_e32 v201, 0
	v_mov_b32_e32 v202, 0
	v_mov_b32_e32 v83, 0
	v_exp_f32_e32 v34, v34
	v_exp_f32_e32 v35, v35
	v_add_f32_e32 v200, v200, v34
	v_exp_f32_e32 v36, v36
	v_add_f32_e32 v201, v201, v35
	v_exp_f32_e32 v37, v37
	s_waitcnt lgkmcnt(7)
	v_mfma_f32_32x32x16_f16 v[2:17], v[168:171], v[108:111], v[130:145]
	v_add_f32_e32 v202, v202, v36
	v_exp_f32_e32 v38, v38
	v_add_f32_e32 v83, v83, v37
	v_exp_f32_e32 v39, v39
	v_add_f32_e32 v200, v200, v38
	v_exp_f32_e32 v40, v40
	s_waitcnt lgkmcnt(6)
	v_mfma_f32_32x32x16_f16 v[18:33], v[172:175], v[108:111], v[130:145]
	v_add_f32_e32 v201, v201, v39
	v_exp_f32_e32 v41, v41
	v_add_f32_e32 v202, v202, v40
	v_exp_f32_e32 v42, v42
	v_add_f32_e32 v83, v83, v41
	v_exp_f32_e32 v43, v43
	s_waitcnt lgkmcnt(5)
	v_mfma_f32_32x32x16_f16 v[2:17], v[176:179], v[104:107], v[2:17]
	v_add_f32_e32 v200, v200, v42
	v_exp_f32_e32 v44, v44
	v_add_f32_e32 v201, v201, v43
	v_exp_f32_e32 v45, v45
	v_add_f32_e32 v202, v202, v44
	v_exp_f32_e32 v46, v46
	s_waitcnt lgkmcnt(4)
	v_mfma_f32_32x32x16_f16 v[18:33], v[180:183], v[104:107], v[18:33]
	v_add_f32_e32 v83, v83, v45
	v_exp_f32_e32 v47, v47
	v_add_f32_e32 v200, v200, v46
	v_exp_f32_e32 v48, v48
	v_add_f32_e32 v201, v201, v47
	v_exp_f32_e32 v49, v49
	s_waitcnt lgkmcnt(3)
	v_mfma_f32_32x32x16_f16 v[2:17], v[184:187], v[100:103], v[2:17]
	v_add_f32_e32 v202, v202, v48
	v_exp_f32_e32 v50, v50
	v_add_f32_e32 v83, v83, v49
	v_exp_f32_e32 v51, v51
	v_add_f32_e32 v200, v200, v50
	v_exp_f32_e32 v52, v52
	s_waitcnt lgkmcnt(2)
	v_mfma_f32_32x32x16_f16 v[18:33], v[188:191], v[100:103], v[18:33]
	v_add_f32_e32 v201, v201, v51
	v_exp_f32_e32 v53, v53
	v_add_f32_e32 v202, v202, v52
	v_exp_f32_e32 v54, v54
	v_add_f32_e32 v83, v83, v53
	v_exp_f32_e32 v55, v55
	s_waitcnt lgkmcnt(1)
	v_mfma_f32_32x32x16_f16 v[2:17], v[192:195], v[96:99], v[2:17]
	v_add_f32_e32 v200, v200, v54
	v_exp_f32_e32 v56, v56
	v_add_f32_e32 v201, v201, v55
	v_exp_f32_e32 v57, v57
	v_add_f32_e32 v202, v202, v56
	v_exp_f32_e32 v58, v58
	s_waitcnt lgkmcnt(0)
	v_mfma_f32_32x32x16_f16 v[18:33], v[196:199], v[96:99], v[18:33]
	ds_read_b128 v[204:207], v167 offset:9216
	ds_read_b128 v[208:211], v167 offset:13824
	ds_read_b128 v[212:215], v167 offset:9248
	ds_read_b128 v[216:219], v167 offset:13856
	ds_read_b128 v[220:223], v167 offset:9280
	ds_read_b128 v[224:227], v167 offset:13888
	ds_read_b128 v[228:231], v167 offset:9312
	ds_read_b128 v[232:235], v167 offset:13920
	v_add_f32_e32 v83, v83, v57
	v_exp_f32_e32 v59, v59
	v_add_f32_e32 v200, v200, v58
	v_exp_f32_e32 v60, v60
	v_add_f32_e32 v201, v201, v59
	v_exp_f32_e32 v61, v61
	v_add_f32_e32 v202, v202, v60
	v_exp_f32_e32 v62, v62
	v_add_f32_e32 v83, v83, v61
	v_exp_f32_e32 v63, v63
	v_add_f32_e32 v200, v200, v62
	v_exp_f32_e32 v64, v64
	v_add_f32_e32 v201, v201, v63
	v_exp_f32_e32 v65, v65
	v_add_f32_e32 v202, v202, v64
	v_add_f32_e32 v83, v83, v65
	v_add_f32_e32 v200, v200, v201
	v_add_f32_e32 v202, v202, v83
	v_add_f32_e32 v200, v200, v202
	v_add_f32_e32 v82, v82, v200
	v_max3_f32 v84, v2, v3, v4
	v_max3_f32 v85, v18, v19, v20
	v_max3_f32 v84, v84, v5, v6
	v_max3_f32 v85, v85, v21, v22
	v_max3_f32 v84, v84, v7, v8
	v_max3_f32 v85, v85, v23, v24
	v_max3_f32 v84, v84, v9, v10
	v_max3_f32 v85, v85, v25, v26
	v_max3_f32 v84, v84, v11, v12
	v_max3_f32 v85, v85, v27, v28
	v_max3_f32 v84, v84, v13, v14
	v_max3_f32 v85, v85, v29, v30
	v_max3_f32 v84, v84, v15, v16
	v_max3_f32 v85, v85, v31, v32
	v_max3_f32 v84, v84, v17, v33
	s_nop 0
	v_max_f32_e32 v84, v84, v85
	s_nop 0
	v_cmp_lt_f32_e32 vcc, s11, v84
	s_cbranch_vccnz .Lp1_rare_d0a

.Lp1_back_d0b:
	s_waitcnt lgkmcnt(0)
	s_barrier
	s_waitcnt vmcnt(2)
	ds_write_b128 v77, v[112:115]
	ds_write_b128 v78, v[116:119]
	ds_write_b128 v77, v[120:123] offset:9216
	ds_write_b128 v78, v[124:127] offset:9216
	global_load_dwordx4 v[146:149], v128, s[24:25]
	global_load_dwordx4 v[150:153], v86, s[24:25]
	s_add_u32 s24, s24, 0x2000
	s_addc_u32 s25, s25, 0
	global_load_dwordx4 v[154:157], v128, s[24:25]
	global_load_dwordx4 v[158:161], v86, s[24:25]
	s_add_u32 s24, s24, 0x2000
	s_addc_u32 s25, s25, 0
	global_store_dwordx4 v90, v[92:95], s[30:31]
	s_add_u32 s30, s30, 0x2000
	s_addc_u32 s31, s31, 0
	global_store_dwordx4 v90, v[92:95], s[30:31]
	s_add_u32 s30, s30, 0x2000
	s_addc_u32 s31, s31, 0
	ds_read_b128 v[168:171], v87
	ds_read_b128 v[172:175], v87 offset:4608
	ds_read_b128 v[176:179], v87 offset:32
	ds_read_b128 v[180:183], v87 offset:4640
	ds_read_b128 v[184:187], v87 offset:64
	ds_read_b128 v[188:191], v87 offset:4672
	ds_read_b128 v[192:195], v87 offset:96
	ds_read_b128 v[196:199], v87 offset:4704
	v_mov_b32_e32 v200, 0
	v_mov_b32_e32 v201, 0
	v_mov_b32_e32 v202, 0
	v_mov_b32_e32 v83, 0
	v_exp_f32_e32 v34, v34
	v_exp_f32_e32 v35, v35
	v_add_f32_e32 v200, v200, v34
	v_exp_f32_e32 v36, v36
	v_add_f32_e32 v201, v201, v35
	v_exp_f32_e32 v37, v37
	s_waitcnt lgkmcnt(7)
	v_mfma_f32_32x32x16_f16 v[2:17], v[168:171], v[108:111], v[130:145]
	v_add_f32_e32 v202, v202, v36
	v_exp_f32_e32 v38, v38
	v_add_f32_e32 v83, v83, v37
	v_exp_f32_e32 v39, v39
	v_add_f32_e32 v200, v200, v38
	v_exp_f32_e32 v40, v40
	s_waitcnt lgkmcnt(6)
	v_mfma_f32_32x32x16_f16 v[18:33], v[172:175], v[108:111], v[130:145]
	v_add_f32_e32 v201, v201, v39
	v_exp_f32_e32 v41, v41
	v_add_f32_e32 v202, v202, v40
	v_exp_f32_e32 v42, v42
	v_add_f32_e32 v83, v83, v41
	v_exp_f32_e32 v43, v43
	s_waitcnt lgkmcnt(5)
	v_mfma_f32_32x32x16_f16 v[2:17], v[176:179], v[104:107], v[2:17]
	v_add_f32_e32 v200, v200, v42
	v_exp_f32_e32 v44, v44
	v_add_f32_e32 v201, v201, v43
	v_exp_f32_e32 v45, v45
	v_add_f32_e32 v202, v202, v44
	v_exp_f32_e32 v46, v46
	s_waitcnt lgkmcnt(4)
	v_mfma_f32_32x32x16_f16 v[18:33], v[180:183], v[104:107], v[18:33]
	v_add_f32_e32 v83, v83, v45
	v_exp_f32_e32 v47, v47
	v_add_f32_e32 v200, v200, v46
	v_exp_f32_e32 v48, v48
	v_add_f32_e32 v201, v201, v47
	v_exp_f32_e32 v49, v49
	s_waitcnt lgkmcnt(3)
	v_mfma_f32_32x32x16_f16 v[2:17], v[184:187], v[100:103], v[2:17]
	v_add_f32_e32 v202, v202, v48
	v_exp_f32_e32 v50, v50
	v_add_f32_e32 v83, v83, v49
	v_exp_f32_e32 v51, v51
	v_add_f32_e32 v200, v200, v50
	v_exp_f32_e32 v52, v52
	s_waitcnt lgkmcnt(2)
	v_mfma_f32_32x32x16_f16 v[18:33], v[188:191], v[100:103], v[18:33]
	v_add_f32_e32 v201, v201, v51
	v_exp_f32_e32 v53, v53
	v_add_f32_e32 v202, v202, v52
	v_exp_f32_e32 v54, v54
	v_add_f32_e32 v83, v83, v53
	v_exp_f32_e32 v55, v55
	s_waitcnt lgkmcnt(1)
	v_mfma_f32_32x32x16_f16 v[2:17], v[192:195], v[96:99], v[2:17]
	v_add_f32_e32 v200, v200, v54
	v_exp_f32_e32 v56, v56
	v_add_f32_e32 v201, v201, v55
	v_exp_f32_e32 v57, v57
	v_add_f32_e32 v202, v202, v56
	v_exp_f32_e32 v58, v58
	s_waitcnt lgkmcnt(0)
	v_mfma_f32_32x32x16_f16 v[18:33], v[196:199], v[96:99], v[18:33]
	ds_read_b128 v[204:207], v87 offset:9216
	ds_read_b128 v[208:211], v87 offset:13824
	ds_read_b128 v[212:215], v87 offset:9248
	ds_read_b128 v[216:219], v87 offset:13856
	ds_read_b128 v[220:223], v87 offset:9280
	ds_read_b128 v[224:227], v87 offset:13888
	ds_read_b128 v[228:231], v87 offset:9312
	ds_read_b128 v[232:235], v87 offset:13920
	v_add_f32_e32 v83, v83, v57
	v_exp_f32_e32 v59, v59
	v_add_f32_e32 v200, v200, v58
	v_exp_f32_e32 v60, v60
	v_add_f32_e32 v201, v201, v59
	v_exp_f32_e32 v61, v61
	v_add_f32_e32 v202, v202, v60
	v_exp_f32_e32 v62, v62
	v_add_f32_e32 v83, v83, v61
	v_exp_f32_e32 v63, v63
	v_add_f32_e32 v200, v200, v62
	v_exp_f32_e32 v64, v64
	v_add_f32_e32 v201, v201, v63
	v_exp_f32_e32 v65, v65
	v_add_f32_e32 v202, v202, v64
	v_add_f32_e32 v83, v83, v65
	v_add_f32_e32 v200, v200, v201
	v_add_f32_e32 v202, v202, v83
	v_add_f32_e32 v200, v200, v202
	v_add_f32_e32 v82, v82, v200
	v_max3_f32 v84, v2, v3, v4
	v_max3_f32 v85, v18, v19, v20
	v_max3_f32 v84, v84, v5, v6
	v_max3_f32 v85, v85, v21, v22
	v_max3_f32 v84, v84, v7, v8
	v_max3_f32 v85, v85, v23, v24
	v_max3_f32 v84, v84, v9, v10
	v_max3_f32 v85, v85, v25, v26
	v_max3_f32 v84, v84, v11, v12
	v_max3_f32 v85, v85, v27, v28
	v_max3_f32 v84, v84, v13, v14
	v_max3_f32 v85, v85, v29, v30
	v_max3_f32 v84, v84, v15, v16
	v_max3_f32 v85, v85, v31, v32
	v_max3_f32 v84, v84, v17, v33
	s_nop 0
	v_max_f32_e32 v84, v84, v85
	s_nop 0
	v_cmp_lt_f32_e32 vcc, s11, v84
	s_cbranch_vccnz .Lp1_rare_d1a
